# LDS bank conflicts: sparse-attention V image plane stride padded 2048->2080 B (wave stride 8320) so the 4 planes written by one 8-lane group no longer share banks (4-way -> 2-way on ds_write_b128)
# speedup vs baseline: 1.0007x; 1.0007x over previous
.LBB0_1359:
	s_or_b64 exec, exec, s[0:1]
	s_lshl_b32 s0, s10, 12
	s_add_i32 s34, s0, 0
	s_add_i32 s14, s34, s0
	s_add_u32 s10, s64, 0x10200000
	s_addc_u32 s11, s65, 0
	s_add_u32 s35, s64, 0x3ba10000
	s_addc_u32 s36, s65, 0
	s_mul_i32 s0, s12, 0xe00
	v_and_b32_e32 v206, 15, v0
	s_mul_hi_i32 s1, s12, 0xe00
	s_add_u32 s0, s10, s0
	s_addc_u32 s1, s11, s1
	v_lshlrev_b32_e32 v70, 7, v206
	v_mov_b32_e32 v71, v3
	s_waitcnt vmcnt(0)
	v_lshlrev_b32_sdwa v10, v232, v8 dst_sel:DWORD dst_unused:UNUSED_PAD src0_sel:DWORD src1_sel:WORD_0
	v_lshlrev_b32_sdwa v11, v232, v8 dst_sel:DWORD dst_unused:UNUSED_PAD src0_sel:DWORD src1_sel:WORD_1
	v_lshlrev_b32_sdwa v12, v232, v9 dst_sel:DWORD dst_unused:UNUSED_PAD src0_sel:DWORD src1_sel:WORD_0
	v_lshlrev_b32_sdwa v13, v232, v9 dst_sel:DWORD dst_unused:UNUSED_PAD src0_sel:DWORD src1_sel:WORD_1
	v_lshl_add_u32 v2, v1, 2, s34
	v_lshl_add_u64 v[8:9], s[0:1], 0, v[70:71]
	v_and_b32_e32 v72, 48, v68
	v_mov_b32_e32 v73, v3
	v_lshl_add_u64 v[8:9], v[8:9], 0, v[72:73]
	v_lshlrev_b32_e32 v74, 2, v206
	ds_write_b128 v2, v[10:13] offset:10496
	ds_write_b128 v2, v[4:7] offset:11520
	v_add_u32_e32 v207, s34, v74
	global_load_dwordx4 v[144:147], v[8:9], off
	global_load_dwordx4 v[140:143], v[8:9], off offset:64
	s_waitcnt lgkmcnt(0)
	v_add_u32_e32 v2, 0x2800, v207
	ds_read2_b32 v[4:5], v2 offset0:64 offset1:80
	s_ashr_i32 s0, s12, 13
	ds_read2_b32 v[12:13], v2 offset0:96 offset1:112
	s_ashr_i32 s1, s0, 31
	s_lshl_b64 s[0:1], s[0:1], 20
	s_add_u32 s12, s35, s0
	v_and_b32_e32 v208, 48, v0
	s_addc_u32 s13, s36, s1
	v_and_b32_e32 v6, 60, v68
	s_waitcnt lgkmcnt(1)
	v_add_u32_e32 v4, v4, v208
	v_add_u32_e32 v5, v5, v208
	v_lshlrev_b32_e32 v14, 4, v68
	v_add_u32_e32 v30, s34, v6
	global_load_dwordx4 v[8:11], v4, s[12:13]
	s_nop 0
	global_load_dwordx4 v[4:7], v5, s[12:13]
	s_waitcnt lgkmcnt(0)
	v_add_u32_e32 v12, v12, v208
	ds_read2_b32 v[20:21], v2 offset0:128 offset1:144
	v_add_u32_e32 v13, v13, v208
	v_and_or_b32 v209, v14, 48, 64
	global_load_dwordx4 v[16:19], v12, s[12:13]
	s_nop 0
	global_load_dwordx4 v[12:15], v13, s[12:13]
	ds_read2_b32 v[28:29], v2 offset0:160 offset1:176
	s_waitcnt lgkmcnt(1)
	v_add_u32_e32 v2, v20, v208
	v_add_u32_e32 v20, v21, v208
	v_add_u32_e32 v54, 0x2800, v30
	global_load_dwordx4 v[24:27], v2, s[12:13]
	s_nop 0
	global_load_dwordx4 v[20:23], v20, s[12:13]
	s_waitcnt lgkmcnt(0)
	v_add_u32_e32 v2, v28, v208
	ds_read2_b32 v[36:37], v54 offset0:64 offset1:80
	v_add_u32_e32 v28, v29, v208
	global_load_dwordx4 v[32:35], v2, s[12:13]
	s_nop 0
	global_load_dwordx4 v[28:31], v28, s[12:13]
	ds_read2_b32 v[44:45], v54 offset0:96 offset1:112
	v_lshrrev_b32_e32 v75, 4, v68
	s_waitcnt lgkmcnt(1)
	v_add_u32_e32 v2, v36, v209
	v_add_u32_e32 v36, v37, v209
	global_load_dwordx4 v[40:43], v2, s[12:13]
	s_nop 0
	global_load_dwordx4 v[36:39], v36, s[12:13]
	s_waitcnt lgkmcnt(0)
	v_add_u32_e32 v2, v44, v209
	ds_read2_b32 v[52:53], v54 offset0:128 offset1:144
	v_add_u32_e32 v44, v45, v209
	global_load_dwordx4 v[48:51], v2, s[12:13]
	s_nop 0
	global_load_dwordx4 v[44:47], v44, s[12:13]
	ds_read2_b32 v[60:61], v54 offset0:160 offset1:176
	v_lshrrev_b32_e32 v210, 2, v68
	s_waitcnt lgkmcnt(1)
	v_add_u32_e32 v2, v52, v209
	v_add_u32_e32 v52, v53, v209
	global_load_dwordx4 v[56:59], v2, s[12:13]
	s_nop 0
	global_load_dwordx4 v[52:55], v52, s[12:13]
	s_waitcnt lgkmcnt(0)
	v_add_u32_e32 v2, v60, v209
	v_add_u32_e32 v60, v61, v209
	global_load_dwordx4 v[64:67], v2, s[12:13]
	s_nop 0
	global_load_dwordx4 v[60:63], v60, s[12:13]
	v_lshlrev_b32_e32 v68, 11, v68
	v_lshl_add_u64 v[70:71], s[10:11], 0, v[70:71]
	v_and_b32_e32 v68, 0x1800, v68
	v_lshl_add_u64 v[212:213], v[70:71], 0, v[72:73]
	v_add_u32_e32 v72, s14, v68
	v_and_b32_e32 v68, 24, v69
	v_and_b32_e32 v73, 0x1e0, v69
	v_lshlrev_b32_e32 v69, 7, v75
	v_lshlrev_b32_e32 v2, 6, v206
	v_lshlrev_b32_e32 v70, 2, v75
	v_add3_u32 v75, s14, v68, v69
	v_lshlrev_b32_e32 v68, 1, v1
	v_mov_b32_e32 v69, v3
	v_mov_b32_e32 v71, v3
	v_lshl_add_u64 v[222:223], s[8:9], 0, v[68:69]
	v_lshl_add_u64 v[68:69], s[64:65], 0, v[2:3]
	v_add_u32_e32 v211, 0, v74
	v_lshlrev_b32_e32 v74, 3, v0
	v_lshl_add_u64 v[68:69], v[68:69], 0, v[70:71]
	s_mov_b64 s[0:1], 0x19200000
	v_and_b32_e32 v74, 0x60, v74
	v_lshl_add_u64 v[172:173], v[68:69], 0, s[0:1]
	s_add_i32 s0, s34, 0x2d00
	s_add_i32 s37, s62, 0x200
	s_sub_i32 s38, 0x3ff, s62
	s_sub_i32 s39, 0x1ff, s62
	v_add_u32_e32 v215, s0, v208
	s_mov_b32 s40, 0
	v_add_u32_e32 v220, v72, v73
	v_add_u32_e32 v221, v75, v74
	v_subrev_u32_e32 v2, s14, v72
	v_lshrrev_b32_e32 v2, 6, v2
	s_lshr_b32 s0, s14, 6
	v_add3_u32 v220, v220, v2, s0
	v_add_u32_e32 v221, s0, v221
	s_mov_b32 s1, 0

.LBB0_1387:
	ds_read_b128 v[160:163], v246
	v_mfma_f32_16x16x32_fp8_fp8 v[164:167], v[8:9], v[174:175], 0
	s_andn2_b64 vcc, exec, s[28:29]
	s_waitcnt lgkmcnt(0)
	v_add_u32_e32 v2, v211, v160
	v_add_u32_e32 v160, v211, v161
	v_add_u32_e32 v161, v211, v162
	v_add_u32_e32 v162, v211, v163
	ds_read_b32 v168, v2 offset:8192
	ds_read_b32 v169, v160 offset:8192
	ds_read_b32 v170, v161 offset:8192
	ds_read_b32 v171, v162 offset:8192
	v_mfma_f32_16x16x32_fp8_fp8 v[160:163], v[10:11], v[176:177], v[164:167]
	s_waitcnt lgkmcnt(2)
	s_nop 6
	v_pk_fma_f32 v[160:161], v[160:161], s[72:73], v[168:169] op_sel_hi:[1,0,1]
	s_waitcnt lgkmcnt(0)
	v_pk_fma_f32 v[162:163], v[162:163], s[72:73], v[170:171] op_sel_hi:[1,0,1]
	s_nop 0
	ds_read_b128 v[164:167], v246 offset:64
	s_waitcnt lgkmcnt(0)
	v_add_u32_e32 v2, v211, v164
	v_add_u32_e32 v169, v211, v165
	v_add_u32_e32 v170, v211, v166
	v_add_u32_e32 v171, v211, v167
	v_mfma_f32_16x16x32_fp8_fp8 v[164:167], v[4:5], v[174:175], 0
	ds_read_b32 v168, v2 offset:8192
	ds_read_b32 v169, v169 offset:8192
	ds_read_b32 v170, v170 offset:8192
	ds_read_b32 v171, v171 offset:8192
	v_mfma_f32_16x16x32_fp8_fp8 v[164:167], v[6:7], v[176:177], v[164:167]
	s_waitcnt lgkmcnt(0)
	s_nop 6
	v_pk_fma_f32 v[166:167], v[166:167], s[72:73], v[170:171] op_sel_hi:[1,0,1]
	v_pk_fma_f32 v[164:165], v[164:165], s[72:73], v[168:169] op_sel_hi:[1,0,1]
	s_nop 0
	ds_read_b128 v[178:181], v246 offset:128
	s_waitcnt lgkmcnt(0)
	v_add_u32_e32 v2, v211, v178
	v_add_u32_e32 v169, v211, v179
	v_add_u32_e32 v170, v211, v180
	v_add_u32_e32 v171, v211, v181
	v_mfma_f32_16x16x32_fp8_fp8 v[178:181], v[16:17], v[174:175], 0
	ds_read_b32 v168, v2 offset:8192
	ds_read_b32 v169, v169 offset:8192
	ds_read_b32 v170, v170 offset:8192
	ds_read_b32 v171, v171 offset:8192
	v_mfma_f32_16x16x32_fp8_fp8 v[178:181], v[18:19], v[176:177], v[178:181]
	s_waitcnt lgkmcnt(0)
	s_nop 6
	v_pk_fma_f32 v[180:181], v[180:181], s[72:73], v[170:171] op_sel_hi:[1,0,1]
	v_pk_fma_f32 v[178:179], v[178:179], s[72:73], v[168:169] op_sel_hi:[1,0,1]
	s_nop 0
	ds_read_b128 v[182:185], v246 offset:192
	s_waitcnt lgkmcnt(0)
	v_add_u32_e32 v2, v211, v182
	v_add_u32_e32 v169, v211, v183
	v_add_u32_e32 v170, v211, v184
	v_add_u32_e32 v171, v211, v185
	v_mfma_f32_16x16x32_fp8_fp8 v[182:185], v[12:13], v[174:175], 0
	ds_read_b32 v168, v2 offset:8192
	ds_read_b32 v169, v169 offset:8192
	ds_read_b32 v170, v170 offset:8192
	ds_read_b32 v171, v171 offset:8192
	v_max3_f32 v2, v160, s33, v161
	v_max3_f32 v2, v2, v162, v163
	v_mfma_f32_16x16x32_fp8_fp8 v[182:185], v[14:15], v[176:177], v[182:185]
	v_max3_f32 v2, v2, v164, v165
	v_max3_f32 v2, v2, v166, v167
	v_max3_f32 v2, v2, v178, v179
	v_max3_f32 v2, v2, v180, v181
	s_waitcnt lgkmcnt(0)
	s_nop 2
	v_pk_fma_f32 v[184:185], v[184:185], s[72:73], v[170:171] op_sel_hi:[1,0,1]
	v_pk_fma_f32 v[182:183], v[182:183], s[72:73], v[168:169] op_sel_hi:[1,0,1]
	s_nop 0
	ds_read_b128 v[186:189], v246 offset:256
	v_max3_f32 v2, v2, v182, v183
	v_max3_f32 v2, v2, v184, v185
	s_waitcnt lgkmcnt(0)
	v_add_u32_e32 v168, v211, v186
	v_add_u32_e32 v169, v211, v187
	v_add_u32_e32 v170, v211, v188
	v_add_u32_e32 v171, v211, v189
	v_mfma_f32_16x16x32_fp8_fp8 v[186:189], v[24:25], v[174:175], 0
	ds_read_b32 v168, v168 offset:8192
	ds_read_b32 v169, v169 offset:8192
	ds_read_b32 v170, v170 offset:8192
	ds_read_b32 v171, v171 offset:8192
	v_mfma_f32_16x16x32_fp8_fp8 v[186:189], v[26:27], v[176:177], v[186:189]
	s_waitcnt lgkmcnt(0)
	s_nop 6
	v_pk_fma_f32 v[236:237], v[188:189], s[72:73], v[170:171] op_sel_hi:[1,0,1]
	v_pk_fma_f32 v[234:235], v[186:187], s[72:73], v[168:169] op_sel_hi:[1,0,1]
	s_nop 0
	ds_read_b128 v[186:189], v246 offset:320
	v_max3_f32 v2, v2, v234, v235
	v_max3_f32 v2, v2, v236, v237
	s_waitcnt lgkmcnt(0)
	v_add_u32_e32 v168, v211, v186
	v_add_u32_e32 v169, v211, v187
	v_add_u32_e32 v170, v211, v188
	v_add_u32_e32 v171, v211, v189
	v_mfma_f32_16x16x32_fp8_fp8 v[186:189], v[20:21], v[174:175], 0
	ds_read_b32 v168, v168 offset:8192
	ds_read_b32 v169, v169 offset:8192
	ds_read_b32 v170, v170 offset:8192
	ds_read_b32 v171, v171 offset:8192
	v_mfma_f32_16x16x32_fp8_fp8 v[186:189], v[22:23], v[176:177], v[186:189]
	s_waitcnt lgkmcnt(0)
	s_nop 6
	v_pk_fma_f32 v[230:231], v[188:189], s[72:73], v[170:171] op_sel_hi:[1,0,1]
	v_pk_fma_f32 v[228:229], v[186:187], s[72:73], v[168:169] op_sel_hi:[1,0,1]
	s_nop 0
	ds_read_b128 v[186:189], v246 offset:384
	v_max3_f32 v2, v2, v228, v229
	v_max3_f32 v2, v2, v230, v231
	s_waitcnt lgkmcnt(0)
	v_add_u32_e32 v168, v211, v186
	v_add_u32_e32 v169, v211, v187
	v_add_u32_e32 v170, v211, v188
	v_add_u32_e32 v171, v211, v189
	v_mfma_f32_16x16x32_fp8_fp8 v[186:189], v[32:33], v[174:175], 0
	ds_read_b32 v168, v168 offset:8192
	ds_read_b32 v169, v169 offset:8192
	ds_read_b32 v170, v170 offset:8192
	ds_read_b32 v171, v171 offset:8192
	v_mfma_f32_16x16x32_fp8_fp8 v[186:189], v[34:35], v[176:177], v[186:189]
	s_waitcnt lgkmcnt(0)
	s_nop 6
	v_pk_fma_f32 v[170:171], v[188:189], s[72:73], v[170:171] op_sel_hi:[1,0,1]
	v_pk_fma_f32 v[168:169], v[186:187], s[72:73], v[168:169] op_sel_hi:[1,0,1]
	s_nop 0
	ds_read_b128 v[186:189], v246 offset:448
	v_max3_f32 v2, v2, v168, v169
	v_max3_f32 v2, v2, v170, v171
	s_waitcnt lgkmcnt(0)
	v_add_u32_e32 v190, v211, v186
	v_add_u32_e32 v191, v211, v187
	v_add_u32_e32 v192, v211, v188
	v_add_u32_e32 v193, v211, v189
	v_mfma_f32_16x16x32_fp8_fp8 v[186:189], v[28:29], v[174:175], 0
	ds_read_b32 v190, v190 offset:8192
	ds_read_b32 v191, v191 offset:8192
	ds_read_b32 v192, v192 offset:8192
	ds_read_b32 v193, v193 offset:8192
	v_mfma_f32_16x16x32_fp8_fp8 v[186:189], v[30:31], v[176:177], v[186:189]
	s_waitcnt lgkmcnt(0)
	s_nop 6
	v_pk_fma_f32 v[218:219], v[188:189], s[72:73], v[192:193] op_sel_hi:[1,0,1]
	v_pk_fma_f32 v[216:217], v[186:187], s[72:73], v[190:191] op_sel_hi:[1,0,1]
	s_nop 0
	s_nop 0
	v_max3_f32 v2, v2, v216, v217
	v_max3_f32 v2, v2, v218, v219
	v_mov_b32_e32 v186, v2
	s_nop 1
	v_permlane16_swap_b32_e32 v2, v186
	v_max_f32_e32 v186, v186, v186
	v_max_f32_e32 v2, v2, v2
	v_max_f32_e32 v2, v2, v186
	v_mov_b32_e32 v186, v2
	s_nop 1
	v_permlane32_swap_b32_e32 v2, v186
	v_max3_f32 v214, v196, v2, v186
	v_sub_f32_e32 v163, v163, v214
	v_sub_f32_e32 v162, v162, v214
	v_sub_f32_e32 v161, v161, v214
	v_sub_f32_e32 v160, v160, v214
	v_sub_f32_e32 v2, v196, v214
	v_exp_f32_e32 v196, v160
	v_exp_f32_e32 v197, v161
	v_exp_f32_e32 v198, v162
	v_exp_f32_e32 v199, v163
	v_sub_f32_e32 v163, v167, v214
	v_sub_f32_e32 v162, v166, v214
	v_sub_f32_e32 v161, v165, v214
	v_sub_f32_e32 v160, v164, v214
	v_sub_f32_e32 v167, v219, v214
	v_exp_f32_e32 v200, v160
	v_exp_f32_e32 v201, v161
	v_exp_f32_e32 v202, v162
	v_exp_f32_e32 v203, v163
	v_sub_f32_e32 v163, v181, v214
	v_sub_f32_e32 v162, v180, v214
	v_sub_f32_e32 v161, v179, v214
	v_sub_f32_e32 v160, v178, v214
	v_sub_f32_e32 v166, v218, v214
	v_exp_f32_e32 v188, v160
	v_exp_f32_e32 v189, v161
	v_exp_f32_e32 v190, v162
	v_exp_f32_e32 v191, v163
	v_sub_f32_e32 v163, v185, v214
	v_sub_f32_e32 v162, v184, v214
	v_sub_f32_e32 v161, v183, v214
	v_sub_f32_e32 v160, v182, v214
	v_sub_f32_e32 v165, v217, v214
	v_exp_f32_e32 v192, v160
	v_exp_f32_e32 v193, v161
	v_exp_f32_e32 v194, v162
	v_exp_f32_e32 v195, v163
	v_sub_f32_e32 v163, v237, v214
	v_sub_f32_e32 v162, v236, v214
	v_sub_f32_e32 v161, v235, v214
	v_sub_f32_e32 v160, v234, v214
	v_sub_f32_e32 v164, v216, v214
	v_exp_f32_e32 v178, v160
	v_exp_f32_e32 v179, v161
	v_exp_f32_e32 v180, v162
	v_exp_f32_e32 v181, v163
	v_sub_f32_e32 v163, v231, v214
	v_sub_f32_e32 v162, v230, v214
	v_sub_f32_e32 v161, v229, v214
	v_sub_f32_e32 v160, v228, v214
	v_pk_add_f32 v[218:219], v[190:191], v[194:195]
	v_exp_f32_e32 v182, v160
	v_exp_f32_e32 v183, v161
	v_exp_f32_e32 v184, v162
	v_exp_f32_e32 v185, v163
	v_sub_f32_e32 v163, v171, v214
	v_sub_f32_e32 v162, v170, v214
	v_sub_f32_e32 v161, v169, v214
	v_sub_f32_e32 v160, v168, v214
	v_pk_add_f32 v[170:171], v[198:199], v[202:203]
	v_exp_f32_e32 v160, v160
	v_exp_f32_e32 v161, v161
	v_exp_f32_e32 v162, v162
	v_exp_f32_e32 v163, v163
	v_exp_f32_e32 v164, v164
	v_exp_f32_e32 v165, v165
	v_exp_f32_e32 v166, v166
	v_exp_f32_e32 v167, v167
	v_pk_add_f32 v[168:169], v[196:197], v[200:201]
	v_pk_add_f32 v[216:217], v[188:189], v[192:193]
	v_pk_add_f32 v[230:231], v[180:181], v[184:185]
	v_pk_add_f32 v[228:229], v[178:179], v[182:183]
	v_pk_add_f32 v[236:237], v[162:163], v[166:167]
	v_pk_add_f32 v[234:235], v[160:161], v[164:165]
	v_exp_f32_e32 v2, v2
	s_nop 0
	v_pk_add_f32 v[170:171], v[170:171], v[218:219]
	v_pk_add_f32 v[168:169], v[168:169], v[216:217]
	v_pk_add_f32 v[218:219], v[230:231], v[236:237]
	v_pk_add_f32 v[216:217], v[228:229], v[234:235]
	v_pk_mul_f32 v[158:159], v[158:159], v[2:3] op_sel_hi:[1,0]
	v_pk_mul_f32 v[156:157], v[156:157], v[2:3] op_sel_hi:[1,0]
	v_pk_add_f32 v[170:171], v[170:171], v[218:219]
	v_pk_add_f32 v[168:169], v[168:169], v[216:217]
	v_cvt_scalef32_pk_bf16_fp8 v217, v42, 1.0 op_sel:[1,0,0]
	v_cvt_scalef32_pk_bf16_fp8 v216, v42, 1.0
	v_pk_add_f32 v[186:187], v[168:169], v[170:171]
	v_cvt_scalef32_pk_bf16_fp8 v169, v40, 1.0 op_sel:[1,0,0]
	v_cvt_scalef32_pk_bf16_fp8 v168, v40, 1.0
	v_cvt_scalef32_pk_bf16_fp8 v171, v41, 1.0 op_sel:[1,0,0]
	v_cvt_scalef32_pk_bf16_fp8 v170, v41, 1.0
	v_cvt_scalef32_pk_bf16_fp8 v218, v43, 1.0
	v_cvt_scalef32_pk_bf16_fp8 v219, v43, 1.0 op_sel:[1,0,0]
	ds_write_b128 v220, v[168:171] offset:43264
	ds_write_b128 v220, v[216:219] offset:43280
	v_cvt_scalef32_pk_bf16_fp8 v169, v36, 1.0 op_sel:[1,0,0]
	v_cvt_scalef32_pk_bf16_fp8 v168, v36, 1.0
	v_cvt_scalef32_pk_bf16_fp8 v171, v37, 1.0 op_sel:[1,0,0]
	v_cvt_scalef32_pk_bf16_fp8 v170, v37, 1.0
	v_cvt_scalef32_pk_bf16_fp8 v217, v38, 1.0 op_sel:[1,0,0]
	v_cvt_scalef32_pk_bf16_fp8 v216, v38, 1.0
	v_cvt_scalef32_pk_bf16_fp8 v218, v39, 1.0
	v_cvt_scalef32_pk_bf16_fp8 v219, v39, 1.0 op_sel:[1,0,0]
	ds_write_b128 v220, v[168:171] offset:43776
	ds_write_b128 v220, v[216:219] offset:43792
	v_cvt_scalef32_pk_bf16_fp8 v169, v48, 1.0 op_sel:[1,0,0]
	v_cvt_scalef32_pk_bf16_fp8 v168, v48, 1.0
	v_cvt_scalef32_pk_bf16_fp8 v171, v49, 1.0 op_sel:[1,0,0]
	v_cvt_scalef32_pk_bf16_fp8 v170, v49, 1.0
	v_cvt_scalef32_pk_bf16_fp8 v217, v50, 1.0 op_sel:[1,0,0]
	v_cvt_scalef32_pk_bf16_fp8 v216, v50, 1.0
	v_cvt_scalef32_pk_bf16_fp8 v218, v51, 1.0
	v_cvt_scalef32_pk_bf16_fp8 v219, v51, 1.0 op_sel:[1,0,0]
	ds_write_b128 v220, v[168:171] offset:44288
	ds_write_b128 v220, v[216:219] offset:44304
	v_cvt_scalef32_pk_bf16_fp8 v169, v44, 1.0 op_sel:[1,0,0]
	v_cvt_scalef32_pk_bf16_fp8 v168, v44, 1.0
	v_cvt_scalef32_pk_bf16_fp8 v171, v45, 1.0 op_sel:[1,0,0]
	v_cvt_scalef32_pk_bf16_fp8 v170, v45, 1.0
	v_cvt_scalef32_pk_bf16_fp8 v217, v46, 1.0 op_sel:[1,0,0]
	v_cvt_scalef32_pk_bf16_fp8 v216, v46, 1.0
	v_cvt_scalef32_pk_bf16_fp8 v218, v47, 1.0
	v_cvt_scalef32_pk_bf16_fp8 v219, v47, 1.0 op_sel:[1,0,0]
	ds_write_b128 v220, v[168:171] offset:44800
	ds_write_b128 v220, v[216:219] offset:44816
	v_cvt_pk_bf16_f32 v168, v196, v197
	v_cvt_pk_bf16_f32 v169, v198, v199
	v_cvt_pk_bf16_f32 v170, v200, v201
	v_cvt_pk_bf16_f32 v171, v202, v203
	ds_read_b64_tr_b16 v[196:197], v221 offset:43264
	ds_read_b64_tr_b16 v[198:199], v221 offset:43776
	ds_read_b64_tr_b16 v[200:201], v221 offset:45344
	ds_read_b64_tr_b16 v[202:203], v221 offset:45856
	ds_read_b64_tr_b16 v[216:217], v221 offset:47424
	ds_read_b64_tr_b16 v[218:219], v221 offset:47936
	s_waitcnt lgkmcnt(4)
	v_mfma_f32_16x16x32_bf16 v[156:159], v[196:199], v[168:171], v[156:159]
	ds_read_b64_tr_b16 v[196:197], v221 offset:49504
	ds_read_b64_tr_b16 v[198:199], v221 offset:50016
	v_pk_mul_f32 v[154:155], v[154:155], v[2:3] op_sel_hi:[1,0]
	v_pk_mul_f32 v[152:153], v[152:153], v[2:3] op_sel_hi:[1,0]
	v_pk_mul_f32 v[150:151], v[150:151], v[2:3] op_sel_hi:[1,0]
	v_pk_mul_f32 v[148:149], v[148:149], v[2:3] op_sel_hi:[1,0]
	v_pk_mul_f32 v[146:147], v[146:147], v[2:3] op_sel_hi:[1,0]
	v_pk_mul_f32 v[144:145], v[144:145], v[2:3] op_sel_hi:[1,0]
	s_waitcnt lgkmcnt(4)
	v_mfma_f32_16x16x32_bf16 v[152:155], v[200:203], v[168:171], v[152:155]
	v_cvt_pk_bf16_f32 v188, v188, v189
	v_cvt_pk_bf16_f32 v189, v190, v191
	v_cvt_pk_bf16_f32 v190, v192, v193
	s_waitcnt lgkmcnt(2)
	v_mfma_f32_16x16x32_bf16 v[148:151], v[216:219], v[168:171], v[148:151]
	v_cvt_pk_bf16_f32 v191, v194, v195
	ds_read_b64_tr_b16 v[192:193], v221 offset:44288
	ds_read_b64_tr_b16 v[194:195], v221 offset:44800
	v_pk_add_f32 v[186:187], v[186:187], v[186:187] op_sel:[0,1] op_sel_hi:[1,0]
	s_waitcnt lgkmcnt(2)
	v_mfma_f32_16x16x32_bf16 v[144:147], v[196:199], v[168:171], v[144:147]
	ds_read_b64_tr_b16 v[168:169], v221 offset:46368
	ds_read_b64_tr_b16 v[170:171], v221 offset:46880
	v_cvt_scalef32_pk_bf16_fp8 v197, v58, 1.0 op_sel:[1,0,0]
	v_cvt_scalef32_pk_bf16_fp8 v196, v58, 1.0
	s_waitcnt lgkmcnt(2)
	v_mfma_f32_16x16x32_bf16 v[156:159], v[192:195], v[188:191], v[156:159]
	v_cvt_scalef32_pk_bf16_fp8 v198, v59, 1.0
	v_cvt_scalef32_pk_bf16_fp8 v199, v59, 1.0 op_sel:[1,0,0]
	s_waitcnt lgkmcnt(0)
	v_mfma_f32_16x16x32_bf16 v[152:155], v[168:171], v[188:191], v[152:155]
	ds_read_b64_tr_b16 v[168:169], v221 offset:48448
	ds_read_b64_tr_b16 v[170:171], v221 offset:48960
	ds_read_b64_tr_b16 v[192:193], v221 offset:50528
	ds_read_b64_tr_b16 v[194:195], v221 offset:51040
	s_waitcnt lgkmcnt(2)
	v_mfma_f32_16x16x32_bf16 v[148:151], v[168:171], v[188:191], v[148:151]
	v_cvt_scalef32_pk_bf16_fp8 v169, v56, 1.0 op_sel:[1,0,0]
	v_cvt_scalef32_pk_bf16_fp8 v168, v56, 1.0
	v_cvt_scalef32_pk_bf16_fp8 v171, v57, 1.0 op_sel:[1,0,0]
	v_cvt_scalef32_pk_bf16_fp8 v170, v57, 1.0
	ds_write_b128 v220, v[168:171] offset:43264
	ds_write_b128 v220, v[196:199] offset:43280
	v_cvt_scalef32_pk_bf16_fp8 v169, v52, 1.0 op_sel:[1,0,0]
	v_cvt_scalef32_pk_bf16_fp8 v168, v52, 1.0
	v_cvt_scalef32_pk_bf16_fp8 v171, v53, 1.0 op_sel:[1,0,0]
	v_cvt_scalef32_pk_bf16_fp8 v170, v53, 1.0
	v_cvt_scalef32_pk_bf16_fp8 v197, v54, 1.0 op_sel:[1,0,0]
	v_cvt_scalef32_pk_bf16_fp8 v196, v54, 1.0
	v_cvt_scalef32_pk_bf16_fp8 v198, v55, 1.0
	v_cvt_scalef32_pk_bf16_fp8 v199, v55, 1.0 op_sel:[1,0,0]
	ds_write_b128 v220, v[168:171] offset:43776
	ds_write_b128 v220, v[196:199] offset:43792
	s_waitcnt vmcnt(1)
	v_cvt_scalef32_pk_bf16_fp8 v169, v64, 1.0 op_sel:[1,0,0]
	v_cvt_scalef32_pk_bf16_fp8 v168, v64, 1.0
	v_cvt_scalef32_pk_bf16_fp8 v171, v65, 1.0 op_sel:[1,0,0]
	v_cvt_scalef32_pk_bf16_fp8 v170, v65, 1.0
	v_cvt_scalef32_pk_bf16_fp8 v197, v66, 1.0 op_sel:[1,0,0]
	v_cvt_scalef32_pk_bf16_fp8 v196, v66, 1.0
	v_cvt_scalef32_pk_bf16_fp8 v198, v67, 1.0
	v_cvt_scalef32_pk_bf16_fp8 v199, v67, 1.0 op_sel:[1,0,0]
	ds_write_b128 v220, v[168:171] offset:44288
	ds_write_b128 v220, v[196:199] offset:44304
	s_waitcnt vmcnt(0)
	v_cvt_scalef32_pk_bf16_fp8 v169, v60, 1.0 op_sel:[1,0,0]
	v_cvt_scalef32_pk_bf16_fp8 v168, v60, 1.0
	v_cvt_scalef32_pk_bf16_fp8 v171, v61, 1.0 op_sel:[1,0,0]
	v_cvt_scalef32_pk_bf16_fp8 v170, v61, 1.0
	v_cvt_scalef32_pk_bf16_fp8 v197, v62, 1.0 op_sel:[1,0,0]
	v_cvt_scalef32_pk_bf16_fp8 v196, v62, 1.0
	v_cvt_scalef32_pk_bf16_fp8 v198, v63, 1.0
	v_cvt_scalef32_pk_bf16_fp8 v199, v63, 1.0 op_sel:[1,0,0]
	ds_write_b128 v220, v[168:171] offset:44800
	ds_write_b128 v220, v[196:199] offset:44816
	v_cvt_pk_bf16_f32 v168, v178, v179
	v_cvt_pk_bf16_f32 v169, v180, v181
	v_cvt_pk_bf16_f32 v170, v182, v183
	v_cvt_pk_bf16_f32 v171, v184, v185
	ds_read_b64_tr_b16 v[178:179], v221 offset:43264
	ds_read_b64_tr_b16 v[180:181], v221 offset:43776
	ds_read_b64_tr_b16 v[182:183], v221 offset:45344
	ds_read_b64_tr_b16 v[184:185], v221 offset:45856
	s_waitcnt lgkmcnt(2)
	v_mfma_f32_16x16x32_bf16 v[156:159], v[178:181], v[168:171], v[156:159]
	s_waitcnt lgkmcnt(0)
	v_mfma_f32_16x16x32_bf16 v[152:155], v[182:185], v[168:171], v[152:155]
	ds_read_b64_tr_b16 v[178:179], v221 offset:47424
	ds_read_b64_tr_b16 v[180:181], v221 offset:47936
	ds_read_b64_tr_b16 v[182:183], v221 offset:49504
	ds_read_b64_tr_b16 v[184:185], v221 offset:50016
	v_mfma_f32_16x16x32_bf16 v[144:147], v[192:195], v[188:191], v[144:147]
	s_waitcnt lgkmcnt(2)
	v_mfma_f32_16x16x32_bf16 v[148:151], v[178:181], v[168:171], v[148:151]
	v_cvt_pk_bf16_f32 v178, v160, v161
	v_cvt_pk_bf16_f32 v179, v162, v163
	v_cvt_pk_bf16_f32 v180, v164, v165
	v_cvt_pk_bf16_f32 v181, v166, v167
	ds_read_b64_tr_b16 v[160:161], v221 offset:44288
	ds_read_b64_tr_b16 v[162:163], v221 offset:44800
	ds_read_b64_tr_b16 v[164:165], v221 offset:46368
	ds_read_b64_tr_b16 v[166:167], v221 offset:46880
	s_waitcnt lgkmcnt(4)
	v_mfma_f32_16x16x32_bf16 v[144:147], v[182:185], v[168:171], v[144:147]
	ds_read_b64_tr_b16 v[168:169], v221 offset:48448
	ds_read_b64_tr_b16 v[170:171], v221 offset:48960
	ds_read_b64_tr_b16 v[182:183], v221 offset:50528
	ds_read_b64_tr_b16 v[184:185], v221 offset:51040
	s_waitcnt lgkmcnt(6)
	v_mfma_f32_16x16x32_bf16 v[156:159], v[160:163], v[178:181], v[156:159]
	v_mov_b32_e32 v160, v186
	s_nop 1
	v_permlane16_swap_b32_e32 v186, v160
	s_waitcnt lgkmcnt(4)
	v_mfma_f32_16x16x32_bf16 v[152:155], v[164:167], v[178:181], v[152:155]
	v_add_f32_e32 v160, v186, v160
	v_mov_b32_e32 v161, v160
	s_nop 1
	v_permlane32_swap_b32_e32 v160, v161
	s_waitcnt lgkmcnt(2)
	v_mfma_f32_16x16x32_bf16 v[148:151], v[168:171], v[178:181], v[148:151]
	s_waitcnt lgkmcnt(0)
	v_mfma_f32_16x16x32_bf16 v[144:147], v[182:185], v[178:181], v[144:147]
	s_cbranch_vccnz .LBB0_1389
	s_branch .Lsb_1389

.Lsb_1387:
	ds_read_b128 v[160:163], v246
	v_mfma_f32_16x16x32_fp8_fp8 v[164:167], v[80:81], v[174:175], 0
	s_andn2_b64 vcc, exec, s[28:29]
	s_waitcnt lgkmcnt(0)
	v_add_u32_e32 v2, v211, v160
	v_add_u32_e32 v160, v211, v161
	v_add_u32_e32 v161, v211, v162
	v_add_u32_e32 v162, v211, v163
	ds_read_b32 v168, v2 offset:8192
	ds_read_b32 v169, v160 offset:8192
	ds_read_b32 v170, v161 offset:8192
	ds_read_b32 v171, v162 offset:8192
	v_mfma_f32_16x16x32_fp8_fp8 v[160:163], v[82:83], v[176:177], v[164:167]
	s_waitcnt lgkmcnt(2)
	s_nop 6
	v_pk_fma_f32 v[160:161], v[160:161], s[72:73], v[168:169] op_sel_hi:[1,0,1]
	s_waitcnt lgkmcnt(0)
	v_pk_fma_f32 v[162:163], v[162:163], s[72:73], v[170:171] op_sel_hi:[1,0,1]
	s_nop 0
	ds_read_b128 v[164:167], v246 offset:64
	s_waitcnt lgkmcnt(0)
	v_add_u32_e32 v2, v211, v164
	v_add_u32_e32 v169, v211, v165
	v_add_u32_e32 v170, v211, v166
	v_add_u32_e32 v171, v211, v167
	v_mfma_f32_16x16x32_fp8_fp8 v[164:167], v[76:77], v[174:175], 0
	ds_read_b32 v168, v2 offset:8192
	ds_read_b32 v169, v169 offset:8192
	ds_read_b32 v170, v170 offset:8192
	ds_read_b32 v171, v171 offset:8192
	v_mfma_f32_16x16x32_fp8_fp8 v[164:167], v[78:79], v[176:177], v[164:167]
	s_waitcnt lgkmcnt(0)
	s_nop 6
	v_pk_fma_f32 v[166:167], v[166:167], s[72:73], v[170:171] op_sel_hi:[1,0,1]
	v_pk_fma_f32 v[164:165], v[164:165], s[72:73], v[168:169] op_sel_hi:[1,0,1]
	s_nop 0
	ds_read_b128 v[178:181], v246 offset:128
	s_waitcnt lgkmcnt(0)
	v_add_u32_e32 v2, v211, v178
	v_add_u32_e32 v169, v211, v179
	v_add_u32_e32 v170, v211, v180
	v_add_u32_e32 v171, v211, v181
	v_mfma_f32_16x16x32_fp8_fp8 v[178:181], v[72:73], v[174:175], 0
	ds_read_b32 v168, v2 offset:8192
	ds_read_b32 v169, v169 offset:8192
	ds_read_b32 v170, v170 offset:8192
	ds_read_b32 v171, v171 offset:8192
	v_mfma_f32_16x16x32_fp8_fp8 v[178:181], v[74:75], v[176:177], v[178:181]
	s_waitcnt lgkmcnt(0)
	s_nop 6
	v_pk_fma_f32 v[180:181], v[180:181], s[72:73], v[170:171] op_sel_hi:[1,0,1]
	v_pk_fma_f32 v[178:179], v[178:179], s[72:73], v[168:169] op_sel_hi:[1,0,1]
	s_nop 0
	ds_read_b128 v[182:185], v246 offset:192
	s_waitcnt lgkmcnt(0)
	v_add_u32_e32 v2, v211, v182
	v_add_u32_e32 v169, v211, v183
	v_add_u32_e32 v170, v211, v184
	v_add_u32_e32 v171, v211, v185
	v_mfma_f32_16x16x32_fp8_fp8 v[182:185], v[68:69], v[174:175], 0
	ds_read_b32 v168, v2 offset:8192
	ds_read_b32 v169, v169 offset:8192
	ds_read_b32 v170, v170 offset:8192
	ds_read_b32 v171, v171 offset:8192
	v_max3_f32 v2, v160, s33, v161
	v_max3_f32 v2, v2, v162, v163
	v_mfma_f32_16x16x32_fp8_fp8 v[182:185], v[70:71], v[176:177], v[182:185]
	v_max3_f32 v2, v2, v164, v165
	v_max3_f32 v2, v2, v166, v167
	v_max3_f32 v2, v2, v178, v179
	v_max3_f32 v2, v2, v180, v181
	s_waitcnt lgkmcnt(0)
	s_nop 2
	v_pk_fma_f32 v[184:185], v[184:185], s[72:73], v[170:171] op_sel_hi:[1,0,1]
	v_pk_fma_f32 v[182:183], v[182:183], s[72:73], v[168:169] op_sel_hi:[1,0,1]
	s_nop 0
	ds_read_b128 v[186:189], v246 offset:256
	v_max3_f32 v2, v2, v182, v183
	v_max3_f32 v2, v2, v184, v185
	s_waitcnt lgkmcnt(0)
	v_add_u32_e32 v168, v211, v186
	v_add_u32_e32 v169, v211, v187
	v_add_u32_e32 v170, v211, v188
	v_add_u32_e32 v171, v211, v189
	v_mfma_f32_16x16x32_fp8_fp8 v[186:189], v[96:97], v[174:175], 0
	ds_read_b32 v168, v168 offset:8192
	ds_read_b32 v169, v169 offset:8192
	ds_read_b32 v170, v170 offset:8192
	ds_read_b32 v171, v171 offset:8192
	v_mfma_f32_16x16x32_fp8_fp8 v[186:189], v[98:99], v[176:177], v[186:189]
	s_waitcnt lgkmcnt(0)
	s_nop 6
	v_pk_fma_f32 v[236:237], v[188:189], s[72:73], v[170:171] op_sel_hi:[1,0,1]
	v_pk_fma_f32 v[234:235], v[186:187], s[72:73], v[168:169] op_sel_hi:[1,0,1]
	s_nop 0
	ds_read_b128 v[186:189], v246 offset:320
	v_max3_f32 v2, v2, v234, v235
	v_max3_f32 v2, v2, v236, v237
	s_waitcnt lgkmcnt(0)
	v_add_u32_e32 v168, v211, v186
	v_add_u32_e32 v169, v211, v187
	v_add_u32_e32 v170, v211, v188
	v_add_u32_e32 v171, v211, v189
	v_mfma_f32_16x16x32_fp8_fp8 v[186:189], v[92:93], v[174:175], 0
	ds_read_b32 v168, v168 offset:8192
	ds_read_b32 v169, v169 offset:8192
	ds_read_b32 v170, v170 offset:8192
	ds_read_b32 v171, v171 offset:8192
	v_mfma_f32_16x16x32_fp8_fp8 v[186:189], v[94:95], v[176:177], v[186:189]
	s_waitcnt lgkmcnt(0)
	s_nop 6
	v_pk_fma_f32 v[230:231], v[188:189], s[72:73], v[170:171] op_sel_hi:[1,0,1]
	v_pk_fma_f32 v[228:229], v[186:187], s[72:73], v[168:169] op_sel_hi:[1,0,1]
	s_nop 0
	ds_read_b128 v[186:189], v246 offset:384
	v_max3_f32 v2, v2, v228, v229
	v_max3_f32 v2, v2, v230, v231
	s_waitcnt lgkmcnt(0)
	v_add_u32_e32 v168, v211, v186
	v_add_u32_e32 v169, v211, v187
	v_add_u32_e32 v170, v211, v188
	v_add_u32_e32 v171, v211, v189
	v_mfma_f32_16x16x32_fp8_fp8 v[186:189], v[88:89], v[174:175], 0
	ds_read_b32 v168, v168 offset:8192
	ds_read_b32 v169, v169 offset:8192
	ds_read_b32 v170, v170 offset:8192
	ds_read_b32 v171, v171 offset:8192
	v_mfma_f32_16x16x32_fp8_fp8 v[186:189], v[90:91], v[176:177], v[186:189]
	s_waitcnt lgkmcnt(0)
	s_nop 6
	v_pk_fma_f32 v[170:171], v[188:189], s[72:73], v[170:171] op_sel_hi:[1,0,1]
	v_pk_fma_f32 v[168:169], v[186:187], s[72:73], v[168:169] op_sel_hi:[1,0,1]
	s_nop 0
	ds_read_b128 v[186:189], v246 offset:448
	v_max3_f32 v2, v2, v168, v169
	v_max3_f32 v2, v2, v170, v171
	s_waitcnt lgkmcnt(0)
	v_add_u32_e32 v190, v211, v186
	v_add_u32_e32 v191, v211, v187
	v_add_u32_e32 v192, v211, v188
	v_add_u32_e32 v193, v211, v189
	v_mfma_f32_16x16x32_fp8_fp8 v[186:189], v[84:85], v[174:175], 0
	ds_read_b32 v190, v190 offset:8192
	ds_read_b32 v191, v191 offset:8192
	ds_read_b32 v192, v192 offset:8192
	ds_read_b32 v193, v193 offset:8192
	v_mfma_f32_16x16x32_fp8_fp8 v[186:189], v[86:87], v[176:177], v[186:189]
	s_waitcnt lgkmcnt(0)
	s_nop 6
	v_pk_fma_f32 v[218:219], v[188:189], s[72:73], v[192:193] op_sel_hi:[1,0,1]
	v_pk_fma_f32 v[216:217], v[186:187], s[72:73], v[190:191] op_sel_hi:[1,0,1]
	s_nop 0
	s_nop 0
	v_max3_f32 v2, v2, v216, v217
	v_max3_f32 v2, v2, v218, v219
	v_mov_b32_e32 v186, v2
	s_nop 1
	v_permlane16_swap_b32_e32 v2, v186
	v_max_f32_e32 v186, v186, v186
	v_max_f32_e32 v2, v2, v2
	v_max_f32_e32 v2, v2, v186
	v_mov_b32_e32 v186, v2
	s_nop 1
	v_permlane32_swap_b32_e32 v2, v186
	v_max3_f32 v214, v196, v2, v186
	v_sub_f32_e32 v163, v163, v214
	v_sub_f32_e32 v162, v162, v214
	v_sub_f32_e32 v161, v161, v214
	v_sub_f32_e32 v160, v160, v214
	v_sub_f32_e32 v2, v196, v214
	v_exp_f32_e32 v196, v160
	v_exp_f32_e32 v197, v161
	v_exp_f32_e32 v198, v162
	v_exp_f32_e32 v199, v163
	v_sub_f32_e32 v163, v167, v214
	v_sub_f32_e32 v162, v166, v214
	v_sub_f32_e32 v161, v165, v214
	v_sub_f32_e32 v160, v164, v214
	v_sub_f32_e32 v167, v219, v214
	v_exp_f32_e32 v200, v160
	v_exp_f32_e32 v201, v161
	v_exp_f32_e32 v202, v162
	v_exp_f32_e32 v203, v163
	v_sub_f32_e32 v163, v181, v214
	v_sub_f32_e32 v162, v180, v214
	v_sub_f32_e32 v161, v179, v214
	v_sub_f32_e32 v160, v178, v214
	v_sub_f32_e32 v166, v218, v214
	v_exp_f32_e32 v188, v160
	v_exp_f32_e32 v189, v161
	v_exp_f32_e32 v190, v162
	v_exp_f32_e32 v191, v163
	v_sub_f32_e32 v163, v185, v214
	v_sub_f32_e32 v162, v184, v214
	v_sub_f32_e32 v161, v183, v214
	v_sub_f32_e32 v160, v182, v214
	v_sub_f32_e32 v165, v217, v214
	v_exp_f32_e32 v192, v160
	v_exp_f32_e32 v193, v161
	v_exp_f32_e32 v194, v162
	v_exp_f32_e32 v195, v163
	v_sub_f32_e32 v163, v237, v214
	v_sub_f32_e32 v162, v236, v214
	v_sub_f32_e32 v161, v235, v214
	v_sub_f32_e32 v160, v234, v214
	v_sub_f32_e32 v164, v216, v214
	v_exp_f32_e32 v178, v160
	v_exp_f32_e32 v179, v161
	v_exp_f32_e32 v180, v162
	v_exp_f32_e32 v181, v163
	v_sub_f32_e32 v163, v231, v214
	v_sub_f32_e32 v162, v230, v214
	v_sub_f32_e32 v161, v229, v214
	v_sub_f32_e32 v160, v228, v214
	v_pk_add_f32 v[218:219], v[190:191], v[194:195]
	v_exp_f32_e32 v182, v160
	v_exp_f32_e32 v183, v161
	v_exp_f32_e32 v184, v162
	v_exp_f32_e32 v185, v163
	v_sub_f32_e32 v163, v171, v214
	v_sub_f32_e32 v162, v170, v214
	v_sub_f32_e32 v161, v169, v214
	v_sub_f32_e32 v160, v168, v214
	v_pk_add_f32 v[170:171], v[198:199], v[202:203]
	v_exp_f32_e32 v160, v160
	v_exp_f32_e32 v161, v161
	v_exp_f32_e32 v162, v162
	v_exp_f32_e32 v163, v163
	v_exp_f32_e32 v164, v164
	v_exp_f32_e32 v165, v165
	v_exp_f32_e32 v166, v166
	v_exp_f32_e32 v167, v167
	v_pk_add_f32 v[168:169], v[196:197], v[200:201]
	v_pk_add_f32 v[216:217], v[188:189], v[192:193]
	v_pk_add_f32 v[230:231], v[180:181], v[184:185]
	v_pk_add_f32 v[228:229], v[178:179], v[182:183]
	v_pk_add_f32 v[236:237], v[162:163], v[166:167]
	v_pk_add_f32 v[234:235], v[160:161], v[164:165]
	v_exp_f32_e32 v2, v2
	s_nop 0
	v_pk_add_f32 v[170:171], v[170:171], v[218:219]
	v_pk_add_f32 v[168:169], v[168:169], v[216:217]
	v_pk_add_f32 v[218:219], v[230:231], v[236:237]
	v_pk_add_f32 v[216:217], v[228:229], v[234:235]
	v_pk_mul_f32 v[158:159], v[158:159], v[2:3] op_sel_hi:[1,0]
	v_pk_mul_f32 v[156:157], v[156:157], v[2:3] op_sel_hi:[1,0]
	v_pk_add_f32 v[170:171], v[170:171], v[218:219]
	v_pk_add_f32 v[168:169], v[168:169], v[216:217]
	v_cvt_scalef32_pk_bf16_fp8 v217, v102, 1.0 op_sel:[1,0,0]
	v_cvt_scalef32_pk_bf16_fp8 v216, v102, 1.0
	v_pk_add_f32 v[186:187], v[168:169], v[170:171]
	v_cvt_scalef32_pk_bf16_fp8 v169, v100, 1.0 op_sel:[1,0,0]
	v_cvt_scalef32_pk_bf16_fp8 v168, v100, 1.0
	v_cvt_scalef32_pk_bf16_fp8 v171, v101, 1.0 op_sel:[1,0,0]
	v_cvt_scalef32_pk_bf16_fp8 v170, v101, 1.0
	v_cvt_scalef32_pk_bf16_fp8 v218, v103, 1.0
	v_cvt_scalef32_pk_bf16_fp8 v219, v103, 1.0 op_sel:[1,0,0]
	ds_write_b128 v220, v[168:171] offset:43264
	ds_write_b128 v220, v[216:219] offset:43280
	v_cvt_scalef32_pk_bf16_fp8 v169, v124, 1.0 op_sel:[1,0,0]
	v_cvt_scalef32_pk_bf16_fp8 v168, v124, 1.0
	v_cvt_scalef32_pk_bf16_fp8 v171, v125, 1.0 op_sel:[1,0,0]
	v_cvt_scalef32_pk_bf16_fp8 v170, v125, 1.0
	v_cvt_scalef32_pk_bf16_fp8 v217, v126, 1.0 op_sel:[1,0,0]
	v_cvt_scalef32_pk_bf16_fp8 v216, v126, 1.0
	v_cvt_scalef32_pk_bf16_fp8 v218, v127, 1.0
	v_cvt_scalef32_pk_bf16_fp8 v219, v127, 1.0 op_sel:[1,0,0]
	ds_write_b128 v220, v[168:171] offset:43776
	ds_write_b128 v220, v[216:219] offset:43792
	v_cvt_scalef32_pk_bf16_fp8 v169, v120, 1.0 op_sel:[1,0,0]
	v_cvt_scalef32_pk_bf16_fp8 v168, v120, 1.0
	v_cvt_scalef32_pk_bf16_fp8 v171, v121, 1.0 op_sel:[1,0,0]
	v_cvt_scalef32_pk_bf16_fp8 v170, v121, 1.0
	v_cvt_scalef32_pk_bf16_fp8 v217, v122, 1.0 op_sel:[1,0,0]
	v_cvt_scalef32_pk_bf16_fp8 v216, v122, 1.0
	v_cvt_scalef32_pk_bf16_fp8 v218, v123, 1.0
	v_cvt_scalef32_pk_bf16_fp8 v219, v123, 1.0 op_sel:[1,0,0]
	ds_write_b128 v220, v[168:171] offset:44288
	ds_write_b128 v220, v[216:219] offset:44304
	v_cvt_scalef32_pk_bf16_fp8 v169, v116, 1.0 op_sel:[1,0,0]
	v_cvt_scalef32_pk_bf16_fp8 v168, v116, 1.0
	v_cvt_scalef32_pk_bf16_fp8 v171, v117, 1.0 op_sel:[1,0,0]
	v_cvt_scalef32_pk_bf16_fp8 v170, v117, 1.0
	v_cvt_scalef32_pk_bf16_fp8 v217, v118, 1.0 op_sel:[1,0,0]
	v_cvt_scalef32_pk_bf16_fp8 v216, v118, 1.0
	v_cvt_scalef32_pk_bf16_fp8 v218, v119, 1.0
	v_cvt_scalef32_pk_bf16_fp8 v219, v119, 1.0 op_sel:[1,0,0]
	ds_write_b128 v220, v[168:171] offset:44800
	ds_write_b128 v220, v[216:219] offset:44816
	v_cvt_pk_bf16_f32 v168, v196, v197
	v_cvt_pk_bf16_f32 v169, v198, v199
	v_cvt_pk_bf16_f32 v170, v200, v201
	v_cvt_pk_bf16_f32 v171, v202, v203
	ds_read_b64_tr_b16 v[196:197], v221 offset:43264
	ds_read_b64_tr_b16 v[198:199], v221 offset:43776
	ds_read_b64_tr_b16 v[200:201], v221 offset:45344
	ds_read_b64_tr_b16 v[202:203], v221 offset:45856
	ds_read_b64_tr_b16 v[216:217], v221 offset:47424
	ds_read_b64_tr_b16 v[218:219], v221 offset:47936
	s_waitcnt lgkmcnt(4)
	v_mfma_f32_16x16x32_bf16 v[156:159], v[196:199], v[168:171], v[156:159]
	ds_read_b64_tr_b16 v[196:197], v221 offset:49504
	ds_read_b64_tr_b16 v[198:199], v221 offset:50016
	v_pk_mul_f32 v[154:155], v[154:155], v[2:3] op_sel_hi:[1,0]
	v_pk_mul_f32 v[152:153], v[152:153], v[2:3] op_sel_hi:[1,0]
	v_pk_mul_f32 v[150:151], v[150:151], v[2:3] op_sel_hi:[1,0]
	v_pk_mul_f32 v[148:149], v[148:149], v[2:3] op_sel_hi:[1,0]
	v_pk_mul_f32 v[146:147], v[146:147], v[2:3] op_sel_hi:[1,0]
	v_pk_mul_f32 v[144:145], v[144:145], v[2:3] op_sel_hi:[1,0]
	s_waitcnt lgkmcnt(4)
	v_mfma_f32_16x16x32_bf16 v[152:155], v[200:203], v[168:171], v[152:155]
	v_cvt_pk_bf16_f32 v188, v188, v189
	v_cvt_pk_bf16_f32 v189, v190, v191
	v_cvt_pk_bf16_f32 v190, v192, v193
	s_waitcnt lgkmcnt(2)
	v_mfma_f32_16x16x32_bf16 v[148:151], v[216:219], v[168:171], v[148:151]
	v_cvt_pk_bf16_f32 v191, v194, v195
	ds_read_b64_tr_b16 v[192:193], v221 offset:44288
	ds_read_b64_tr_b16 v[194:195], v221 offset:44800
	v_pk_add_f32 v[186:187], v[186:187], v[186:187] op_sel:[0,1] op_sel_hi:[1,0]
	s_waitcnt lgkmcnt(2)
	v_mfma_f32_16x16x32_bf16 v[144:147], v[196:199], v[168:171], v[144:147]
	ds_read_b64_tr_b16 v[168:169], v221 offset:46368
	ds_read_b64_tr_b16 v[170:171], v221 offset:46880
	v_cvt_scalef32_pk_bf16_fp8 v197, v114, 1.0 op_sel:[1,0,0]
	v_cvt_scalef32_pk_bf16_fp8 v196, v114, 1.0
	s_waitcnt lgkmcnt(2)
	v_mfma_f32_16x16x32_bf16 v[156:159], v[192:195], v[188:191], v[156:159]
	v_cvt_scalef32_pk_bf16_fp8 v198, v115, 1.0
	v_cvt_scalef32_pk_bf16_fp8 v199, v115, 1.0 op_sel:[1,0,0]
	s_waitcnt lgkmcnt(0)
	v_mfma_f32_16x16x32_bf16 v[152:155], v[168:171], v[188:191], v[152:155]
	ds_read_b64_tr_b16 v[168:169], v221 offset:48448
	ds_read_b64_tr_b16 v[170:171], v221 offset:48960
	ds_read_b64_tr_b16 v[192:193], v221 offset:50528
	ds_read_b64_tr_b16 v[194:195], v221 offset:51040
	s_waitcnt lgkmcnt(2)
	v_mfma_f32_16x16x32_bf16 v[148:151], v[168:171], v[188:191], v[148:151]
	v_cvt_scalef32_pk_bf16_fp8 v169, v112, 1.0 op_sel:[1,0,0]
	v_cvt_scalef32_pk_bf16_fp8 v168, v112, 1.0
	v_cvt_scalef32_pk_bf16_fp8 v171, v113, 1.0 op_sel:[1,0,0]
	v_cvt_scalef32_pk_bf16_fp8 v170, v113, 1.0
	ds_write_b128 v220, v[168:171] offset:43264
	ds_write_b128 v220, v[196:199] offset:43280
	v_cvt_scalef32_pk_bf16_fp8 v169, v108, 1.0 op_sel:[1,0,0]
	v_cvt_scalef32_pk_bf16_fp8 v168, v108, 1.0
	v_cvt_scalef32_pk_bf16_fp8 v171, v109, 1.0 op_sel:[1,0,0]
	v_cvt_scalef32_pk_bf16_fp8 v170, v109, 1.0
	v_cvt_scalef32_pk_bf16_fp8 v197, v110, 1.0 op_sel:[1,0,0]
	v_cvt_scalef32_pk_bf16_fp8 v196, v110, 1.0
	v_cvt_scalef32_pk_bf16_fp8 v198, v111, 1.0
	v_cvt_scalef32_pk_bf16_fp8 v199, v111, 1.0 op_sel:[1,0,0]
	ds_write_b128 v220, v[168:171] offset:43776
	ds_write_b128 v220, v[196:199] offset:43792
	s_waitcnt vmcnt(1)
	v_cvt_scalef32_pk_bf16_fp8 v169, v104, 1.0 op_sel:[1,0,0]
	v_cvt_scalef32_pk_bf16_fp8 v168, v104, 1.0
	v_cvt_scalef32_pk_bf16_fp8 v171, v105, 1.0 op_sel:[1,0,0]
	v_cvt_scalef32_pk_bf16_fp8 v170, v105, 1.0
	v_cvt_scalef32_pk_bf16_fp8 v197, v106, 1.0 op_sel:[1,0,0]
	v_cvt_scalef32_pk_bf16_fp8 v196, v106, 1.0
	v_cvt_scalef32_pk_bf16_fp8 v198, v107, 1.0
	v_cvt_scalef32_pk_bf16_fp8 v199, v107, 1.0 op_sel:[1,0,0]
	ds_write_b128 v220, v[168:171] offset:44288
	ds_write_b128 v220, v[196:199] offset:44304
	s_waitcnt vmcnt(0)
	v_cvt_scalef32_pk_bf16_fp8 v169, v128, 1.0 op_sel:[1,0,0]
	v_cvt_scalef32_pk_bf16_fp8 v168, v128, 1.0
	v_cvt_scalef32_pk_bf16_fp8 v171, v129, 1.0 op_sel:[1,0,0]
	v_cvt_scalef32_pk_bf16_fp8 v170, v129, 1.0
	v_cvt_scalef32_pk_bf16_fp8 v197, v130, 1.0 op_sel:[1,0,0]
	v_cvt_scalef32_pk_bf16_fp8 v196, v130, 1.0
	v_cvt_scalef32_pk_bf16_fp8 v198, v131, 1.0
	v_cvt_scalef32_pk_bf16_fp8 v199, v131, 1.0 op_sel:[1,0,0]
	ds_write_b128 v220, v[168:171] offset:44800
	ds_write_b128 v220, v[196:199] offset:44816
	v_cvt_pk_bf16_f32 v168, v178, v179
	v_cvt_pk_bf16_f32 v169, v180, v181
	v_cvt_pk_bf16_f32 v170, v182, v183
	v_cvt_pk_bf16_f32 v171, v184, v185
	ds_read_b64_tr_b16 v[178:179], v221 offset:43264
	ds_read_b64_tr_b16 v[180:181], v221 offset:43776
	ds_read_b64_tr_b16 v[182:183], v221 offset:45344
	ds_read_b64_tr_b16 v[184:185], v221 offset:45856
	s_waitcnt lgkmcnt(2)
	v_mfma_f32_16x16x32_bf16 v[156:159], v[178:181], v[168:171], v[156:159]
	s_waitcnt lgkmcnt(0)
	v_mfma_f32_16x16x32_bf16 v[152:155], v[182:185], v[168:171], v[152:155]
	ds_read_b64_tr_b16 v[178:179], v221 offset:47424
	ds_read_b64_tr_b16 v[180:181], v221 offset:47936
	ds_read_b64_tr_b16 v[182:183], v221 offset:49504
	ds_read_b64_tr_b16 v[184:185], v221 offset:50016
	v_mfma_f32_16x16x32_bf16 v[144:147], v[192:195], v[188:191], v[144:147]
	s_waitcnt lgkmcnt(2)
	v_mfma_f32_16x16x32_bf16 v[148:151], v[178:181], v[168:171], v[148:151]
	v_cvt_pk_bf16_f32 v178, v160, v161
	v_cvt_pk_bf16_f32 v179, v162, v163
	v_cvt_pk_bf16_f32 v180, v164, v165
	v_cvt_pk_bf16_f32 v181, v166, v167
	ds_read_b64_tr_b16 v[160:161], v221 offset:44288
	ds_read_b64_tr_b16 v[162:163], v221 offset:44800
	ds_read_b64_tr_b16 v[164:165], v221 offset:46368
	ds_read_b64_tr_b16 v[166:167], v221 offset:46880
	s_waitcnt lgkmcnt(4)
	v_mfma_f32_16x16x32_bf16 v[144:147], v[182:185], v[168:171], v[144:147]
	ds_read_b64_tr_b16 v[168:169], v221 offset:48448
	ds_read_b64_tr_b16 v[170:171], v221 offset:48960
	ds_read_b64_tr_b16 v[182:183], v221 offset:50528
	ds_read_b64_tr_b16 v[184:185], v221 offset:51040
	s_waitcnt lgkmcnt(6)
	v_mfma_f32_16x16x32_bf16 v[156:159], v[160:163], v[178:181], v[156:159]
	v_mov_b32_e32 v160, v186
	s_nop 1
	v_permlane16_swap_b32_e32 v186, v160
	s_waitcnt lgkmcnt(4)
	v_mfma_f32_16x16x32_bf16 v[152:155], v[164:167], v[178:181], v[152:155]
	v_add_f32_e32 v160, v186, v160
	v_mov_b32_e32 v161, v160
	s_nop 1
	v_permlane32_swap_b32_e32 v160, v161
	s_waitcnt lgkmcnt(2)
	v_mfma_f32_16x16x32_bf16 v[148:151], v[168:171], v[178:181], v[148:151]
	s_waitcnt lgkmcnt(0)
	v_mfma_f32_16x16x32_bf16 v[144:147], v[182:185], v[178:181], v[144:147]
	s_cbranch_vccnz .Lsb_1389
	s_branch .LBB0_1389
